# g1_gather_index_loads_batched
# speedup vs baseline: 1.0077x; 1.0015x over previous
; #define PG8_VOFFA(dst, u) do { if constexpr (GATHER) { _Pragma("unroll") for (int _h = 0; _h < 2; ++_h) _Pragma("unroll") for (int _i = 0; _i < 2; ++_i) { \
;         int _R, _C; stage_rc(tid * 16 + _i * 8192, _R, _C); const int _r = _h * HALF + _R; const int _t = (_r < (u).nvalid) ? (u).gidx[_r] : 0; dst[_h][_i] = (unsigned)(_t * lda + _C) * 2u; } } } while (0)
; template <class Epi, class Sched, bool GATHER, bool ALIGN_EPI>
; __device__ __forceinline__ void gemm_phase(LAS unsigned char* lds, const int wave_, const int K, const int lda, const int ldb, const Sched& S, const Epi& E) {
;     ...
;         const bool has_next = S.next(ui + 1, nxt);
;         if constexpr (GATHER) {
;             if (has_next) { PG8_VOFFA(voffAn, nxt); }
.LBB0_1485:
	v_cndmask_b32_e64 v128, 0, 1, s[22:23]
	v_cmp_ne_u32_e64 s[10:11], 1, v128
	s_andn2_b64 vcc, exec, s[22:23]
	s_mov_b64 s[24:25], s[12:13]
	s_mov_b64 s[22:23], s[4:5]
	v_mov_b32_e32 v198, v172
	v_mov_b32_e32 v197, v164
	v_mov_b32_e32 v199, v168
	v_mov_b32_e32 v200, v170
	s_cbranch_vccnz .LBB0_1495
	v_mov_b32_e32 v132, 0
	v_mov_b32_e32 v133, 0
	v_mov_b32_e32 v134, 0
	v_mov_b32_e32 v135, 0
	v_lshl_add_u64 v[128:129], v[152:153], 2, s[16:17]
	v_lshl_add_u64 v[130:131], v[154:155], 2, s[16:17]
	v_cmp_gt_i32_e32 vcc, s46, v152
	s_and_saveexec_b64 s[22:23], vcc
	global_load_dword v133, v[128:129], off
	s_or_b64 exec, exec, s[22:23]
	v_cmp_gt_i32_e32 vcc, s46, v154
	s_and_saveexec_b64 s[22:23], vcc
	global_load_dword v132, v[130:131], off
	s_or_b64 exec, exec, s[22:23]
	v_cmp_gt_i32_e32 vcc, s46, v163
	s_and_saveexec_b64 s[22:23], vcc
	global_load_dword v135, v[128:129], off offset:512
	s_or_b64 exec, exec, s[22:23]
	v_cmp_gt_i32_e32 vcc, s46, v180
	s_and_saveexec_b64 s[22:23], vcc
	global_load_dword v134, v[130:131], off offset:512
	s_or_b64 exec, exec, s[22:23]
	s_waitcnt vmcnt(0)
	v_lshlrev_b32_e32 v133, 10, v133
	v_lshlrev_b32_e32 v132, 10, v132
	v_lshlrev_b32_e32 v135, 10, v135
	v_lshlrev_b32_e32 v134, 10, v134
	v_readlane_b32 s24, v252, 8
	v_add_lshl_u32 v197, v135, v181, 1
	v_add_lshl_u32 v199, v132, v182, 1
	v_add_lshl_u32 v200, v133, v181, 1
	v_add_lshl_u32 v198, v134, v182, 1
	v_readlane_b32 s25, v252, 9
	s_mov_b64 s[22:23], s[18:19]

; template <int M> __device__ __forceinline__ float swz_xor(float v) { return __int_as_float(__builtin_amdgcn_ds_swizzle(__float_as_int(v), (M << 10) | 0x1f)); }
; __device__ __forceinline__ float half_sum(float v) { auto rr = __builtin_amdgcn_permlane32_swap(__float_as_uint(v), __float_as_uint(v), false, false); return __uint_as_float(rr[0]) + __uint_as_float(rr[1]); }
; __device__ __forceinline__ void row_rscale8(const float* part, const int (&rows)[2][4], int fq, float (&rs)[2][4]) {
;     ...
;         for (int m = 0; m < 4; ++m) v[ai][m] = *(const f32x4*)(part + (size_t)rows[ai][m] * 16 + fq * 4);
; #pragma unroll
;     for (int ai = 0; ai < 2; ++ai)
; #pragma unroll
;         for (int m = 0; m < 4; ++m) { float s = (v[ai][m][0] + v[ai][m][1]) + (v[ai][m][2] + v[ai][m][3]); s += swz_xor<16>(s); s = half_sum(s); rs[ai][m] = __builtin_amdgcn_rcpf(sqrtf(s * (1.0f / DM) + EPS)); }
;     __device__ __forceinline__ bool operator()(f32x4 (&acc)[2][2][4][2], const pg8::Unit& u, int wr, int wc, int fr, int fq) const {
;     ...
;         float rs_[2][4]; { int rows_[2][4];
; #pragma unroll
;             for (int ai = 0; ai < 2; ++ai)
; #pragma unroll
;                 for (int m = 0; m < 4; ++m) { const int rl = ai * 128 + wr * 64 + m * 16 + fr; rows_[ai][m] = (rl < u.nvalid) ? u.gidx[rl] : 0; }
;             row_rscale8(part, rows_, fq, rs_); }
.LBB0_1499:
	v_lshlrev_b32_e32 v140, 2, v162
	v_mov_b32_e32 v216, 0
	v_mov_b32_e32 v218, 0
	v_mov_b32_e32 v220, 0
	v_mov_b32_e32 v222, 0
	v_mov_b32_e32 v224, 0
	v_mov_b32_e32 v226, 0
	v_mov_b32_e32 v228, 0
	v_mov_b32_e32 v232, 0
	v_cmp_gt_i32_e32 vcc, s36, v162
	s_and_saveexec_b64 s[4:5], vcc
	global_load_dword v216, v140, s[6:7]
	s_or_b64 exec, exec, s[4:5]
	v_cmp_gt_i32_e32 vcc, s36, v171
	s_and_saveexec_b64 s[4:5], vcc
	global_load_dword v218, v140, s[6:7] offset:64
	s_or_b64 exec, exec, s[4:5]
	v_cmp_gt_i32_e32 vcc, s36, v183
	s_and_saveexec_b64 s[4:5], vcc
	global_load_dword v220, v140, s[6:7] offset:128
	s_or_b64 exec, exec, s[4:5]
	v_cmp_gt_i32_e32 vcc, s36, v201
	s_and_saveexec_b64 s[4:5], vcc
	global_load_dword v222, v140, s[6:7] offset:192
	s_or_b64 exec, exec, s[4:5]
	v_cmp_gt_i32_e32 vcc, s36, v213
	s_and_saveexec_b64 s[4:5], vcc
	global_load_dword v224, v140, s[6:7] offset:512
	s_or_b64 exec, exec, s[4:5]
	v_cmp_gt_i32_e32 vcc, s36, v186
	s_and_saveexec_b64 s[4:5], vcc
	global_load_dword v226, v140, s[6:7] offset:576
	s_or_b64 exec, exec, s[4:5]
	v_cmp_gt_i32_e32 vcc, s36, v187
	s_and_saveexec_b64 s[4:5], vcc
	global_load_dword v228, v140, s[6:7] offset:640
	s_or_b64 exec, exec, s[4:5]
	v_cmp_gt_i32_e32 vcc, s36, v188
	s_and_saveexec_b64 s[4:5], vcc
	global_load_dword v232, v140, s[6:7] offset:704
	s_or_b64 exec, exec, s[4:5]
	v_mov_b64_e32 v[236:237], v[246:247]
	v_mov_b64_e32 v[230:231], v[184:185]
	s_waitcnt vmcnt(0)
	v_ashrrev_i32_e32 v217, 31, v216
	v_ashrrev_i32_e32 v219, 31, v218
	v_ashrrev_i32_e32 v221, 31, v220
	v_ashrrev_i32_e32 v223, 31, v222
	v_ashrrev_i32_e32 v225, 31, v224
	v_ashrrev_i32_e32 v227, 31, v226
	v_ashrrev_i32_e32 v229, 31, v228
	v_ashrrev_i32_e32 v233, 31, v232
	v_lshlrev_b64 v[130:131], 6, v[216:217]
	v_lshlrev_b64 v[128:129], 6, v[218:219]
	v_lshlrev_b64 v[134:135], 6, v[220:221]
	v_lshlrev_b64 v[132:133], 6, v[222:223]
	v_lshlrev_b64 v[138:139], 6, v[224:225]
	v_lshlrev_b64 v[136:137], 6, v[226:227]
	v_lshlrev_b64 v[178:179], 6, v[228:229]
	v_lshlrev_b64 v[176:177], 6, v[232:233]
	v_lshl_add_u64 v[130:131], v[166:167], 0, v[130:131]
	global_load_dwordx4 v[190:193], v[130:131], off
	v_lshl_add_u64 v[128:129], v[166:167], 0, v[128:129]
	global_load_dwordx4 v[202:205], v[128:129], off
	v_lshl_add_u64 v[128:129], v[166:167], 0, v[134:135]
	global_load_dwordx4 v[148:151], v[128:129], off
	v_lshl_add_u64 v[128:129], v[166:167], 0, v[132:133]
	global_load_dwordx4 v[144:147], v[128:129], off
	v_lshl_add_u64 v[128:129], v[166:167], 0, v[138:139]
	global_load_dwordx4 v[140:143], v[128:129], off
	v_lshl_add_u64 v[128:129], v[166:167], 0, v[136:137]
	global_load_dwordx4 v[136:139], v[128:129], off
	v_lshl_add_u64 v[128:129], v[166:167], 0, v[178:179]
	global_load_dwordx4 v[132:135], v[128:129], off
	v_lshl_add_u64 v[128:129], v[166:167], 0, v[176:177]
	s_mov_b32 s2, 0xf800000
	global_load_dwordx4 v[128:131], v[128:129], off
	v_lshl_or_b32 v174, s45, 7, v189
	s_waitcnt vmcnt(0)
	v_mov_b32_e32 v176, v191
	v_mov_b32_e32 v177, v192
	v_mov_b32_e32 v191, v193
	v_pk_add_f32 v[176:177], v[176:177], v[190:191]
	v_mov_b32_e32 v178, v203
	v_add_f32_e32 v160, v176, v177
	ds_swizzle_b32 v165, v160 offset:swizzle(SWAP,16)
	v_mov_b32_e32 v179, v204
	v_mov_b32_e32 v203, v205
	v_pk_add_f32 v[178:179], v[178:179], v[202:203]
	s_waitcnt lgkmcnt(0)
	v_add_f32_e32 v160, v160, v165
	v_mov_b32_e32 v165, v160
	s_nop 1
	v_permlane32_swap_b32_e32 v160, v165
	v_add_f32_e32 v160, v160, v165
	v_fmamk_f32 v160, v160, 0x3a800000, v212
	v_cmp_gt_f32_e32 vcc, s2, v160
	v_mul_f32_e32 v165, 0x4f800000, v160
	s_nop 0
	v_cndmask_b32_e32 v160, v160, v165, vcc
	v_sqrt_f32_e32 v165, v160
	s_nop 0
	v_add_u32_e32 v173, -1, v165
	v_fma_f32 v175, -v173, v165, v160
	v_cmp_ge_f32_e64 s[4:5], 0, v175
	v_add_u32_e32 v175, 1, v165
	s_nop 0
	v_cndmask_b32_e64 v173, v165, v173, s[4:5]
	v_fma_f32 v165, -v175, v165, v160
	v_cmp_lt_f32_e64 s[4:5], 0, v165
	s_nop 1
	v_cndmask_b32_e64 v165, v173, v175, s[4:5]
	v_mul_f32_e32 v173, 0x37800000, v165
	v_cndmask_b32_e32 v165, v165, v173, vcc
	v_cmp_class_f32_e32 vcc, v160, v248
	s_nop 1
	v_cndmask_b32_e32 v160, v165, v160, vcc
	v_rcp_f32_e32 v176, v160
	v_add_f32_e32 v160, v178, v179
	ds_swizzle_b32 v165, v160 offset:swizzle(SWAP,16)
	v_mov_b32_e32 v178, v149
	v_mov_b32_e32 v179, v150
	v_mov_b32_e32 v149, v151
	v_pk_add_f32 v[148:149], v[178:179], v[148:149]
	s_waitcnt lgkmcnt(0)
	v_add_f32_e32 v160, v160, v165
	v_mov_b32_e32 v165, v160
	s_nop 1
	v_permlane32_swap_b32_e32 v160, v165
	v_add_f32_e32 v160, v160, v165
	v_fmamk_f32 v160, v160, 0x3a800000, v212
	v_cmp_gt_f32_e32 vcc, s2, v160
	v_mul_f32_e32 v165, 0x4f800000, v160
	v_add_f32_e32 v148, v148, v149
	v_cndmask_b32_e32 v160, v160, v165, vcc
	v_sqrt_f32_e32 v165, v160
	ds_swizzle_b32 v149, v148 offset:swizzle(SWAP,16)
	v_add_u32_e32 v173, -1, v165
	v_fma_f32 v175, -v173, v165, v160
	v_cmp_ge_f32_e64 s[4:5], 0, v175
	v_add_u32_e32 v175, 1, v165
	s_waitcnt lgkmcnt(0)
; template <int M> __device__ __forceinline__ float swz_xor(float v) { return __int_as_float(__builtin_amdgcn_ds_swizzle(__float_as_int(v), (M << 10) | 0x1f)); }
; __device__ __forceinline__ float half_sum(float v) { auto rr = __builtin_amdgcn_permlane32_swap(__float_as_uint(v), __float_as_uint(v), false, false); return __uint_as_float(rr[0]) + __uint_as_float(rr[1]); }
; __device__ __forceinline__ void row_rscale8(const float* part, const int (&rows)[2][4], int fq, float (&rs)[2][4]) {
;     ...
;         for (int m = 0; m < 4; ++m) v[ai][m] = *(const f32x4*)(part + (size_t)rows[ai][m] * 16 + fq * 4);
; #pragma unroll
;     for (int ai = 0; ai < 2; ++ai)
; #pragma unroll
;         for (int m = 0; m < 4; ++m) { float s = (v[ai][m][0] + v[ai][m][1]) + (v[ai][m][2] + v[ai][m][3]); s += swz_xor<16>(s); s = half_sum(s); rs[ai][m] = __builtin_amdgcn_rcpf(sqrtf(s * (1.0f / DM) + EPS)); }
	v_add_f32_e32 v148, v148, v149
	v_cndmask_b32_e64 v173, v165, v173, s[4:5]
	v_fma_f32 v165, -v175, v165, v160
	v_cmp_lt_f32_e64 s[4:5], 0, v165
	v_mov_b32_e32 v149, v148
	s_nop 1
	v_permlane32_swap_b32_e32 v148, v149
	v_cndmask_b32_e64 v165, v173, v175, s[4:5]
	v_mul_f32_e32 v173, 0x37800000, v165
	v_add_f32_e32 v148, v148, v149
	v_cndmask_b32_e32 v165, v165, v173, vcc
	v_cmp_class_f32_e32 vcc, v160, v248
	v_fmamk_f32 v148, v148, 0x3a800000, v212
	v_mul_f32_e32 v149, 0x4f800000, v148
	v_cndmask_b32_e32 v160, v165, v160, vcc
	v_cmp_gt_f32_e32 vcc, s2, v148
	v_rcp_f32_e32 v160, v160
	v_ashrrev_i32_e32 v175, 31, v174
	v_cndmask_b32_e32 v148, v148, v149, vcc
	v_sqrt_f32_e32 v149, v148
	s_nop 0
	v_add_u32_e32 v150, -1, v149
	v_fma_f32 v151, -v150, v149, v148
	v_cmp_ge_f32_e64 s[4:5], 0, v151
	v_add_u32_e32 v151, 1, v149
	s_nop 0
	v_cndmask_b32_e64 v150, v149, v150, s[4:5]
	v_fma_f32 v149, -v151, v149, v148
	v_cmp_lt_f32_e64 s[4:5], 0, v149
	s_nop 1
	v_cndmask_b32_e64 v149, v150, v151, s[4:5]
	v_mul_f32_e32 v150, 0x37800000, v149
	v_cndmask_b32_e32 v149, v149, v150, vcc
	v_mov_b32_e32 v150, v145
	v_mov_b32_e32 v151, v146
	v_mov_b32_e32 v145, v147
	v_pk_add_f32 v[144:145], v[150:151], v[144:145]
	v_cmp_class_f32_e32 vcc, v148, v248
	v_add_f32_e32 v144, v144, v145
	ds_swizzle_b32 v145, v144 offset:swizzle(SWAP,16)
	v_cndmask_b32_e32 v148, v149, v148, vcc
	v_rcp_f32_e32 v148, v148
	s_waitcnt lgkmcnt(0)
	v_add_f32_e32 v144, v144, v145
	v_mov_b32_e32 v145, v144
	s_nop 1
	v_permlane32_swap_b32_e32 v144, v145
	v_add_f32_e32 v144, v144, v145
	v_fmamk_f32 v144, v144, 0x3a800000, v212
	v_cmp_gt_f32_e32 vcc, s2, v144
	v_mul_f32_e32 v145, 0x4f800000, v144
	s_nop 0
	v_cndmask_b32_e32 v144, v144, v145, vcc
	v_sqrt_f32_e32 v145, v144
	s_nop 0
	v_add_u32_e32 v146, -1, v145
	v_fma_f32 v147, -v146, v145, v144
	v_cmp_ge_f32_e64 s[4:5], 0, v147
	v_add_u32_e32 v147, 1, v145
	s_nop 0
	v_cndmask_b32_e64 v146, v145, v146, s[4:5]
	v_fma_f32 v145, -v147, v145, v144
	v_cmp_lt_f32_e64 s[4:5], 0, v145
	s_nop 1
	v_cndmask_b32_e64 v145, v146, v147, s[4:5]
	v_mul_f32_e32 v146, 0x37800000, v145
	v_cndmask_b32_e32 v145, v145, v146, vcc
	v_mov_b32_e32 v146, v141
	v_mov_b32_e32 v147, v142
	v_mov_b32_e32 v141, v143
	v_pk_add_f32 v[140:141], v[146:147], v[140:141]
	v_cmp_class_f32_e32 vcc, v144, v248
	v_add_f32_e32 v140, v140, v141
	ds_swizzle_b32 v141, v140 offset:swizzle(SWAP,16)
	v_cndmask_b32_e32 v144, v145, v144, vcc
	v_rcp_f32_e32 v144, v144
	s_waitcnt lgkmcnt(0)
	v_add_f32_e32 v140, v140, v141
	v_mov_b32_e32 v141, v140
	s_nop 1
	v_permlane32_swap_b32_e32 v140, v141
	v_add_f32_e32 v140, v140, v141
	v_fmamk_f32 v140, v140, 0x3a800000, v212
	v_cmp_gt_f32_e32 vcc, s2, v140
	v_mul_f32_e32 v141, 0x4f800000, v140
	s_nop 0
	v_cndmask_b32_e32 v140, v140, v141, vcc
	v_sqrt_f32_e32 v141, v140
	s_nop 0
	v_add_u32_e32 v142, -1, v141
	v_fma_f32 v143, -v142, v141, v140
	v_cmp_ge_f32_e64 s[4:5], 0, v143
	v_add_u32_e32 v143, 1, v141
	s_nop 0
	v_cndmask_b32_e64 v142, v141, v142, s[4:5]
	v_fma_f32 v141, -v143, v141, v140
	v_cmp_lt_f32_e64 s[4:5], 0, v141
	s_nop 1
	v_cndmask_b32_e64 v141, v142, v143, s[4:5]
	v_mul_f32_e32 v142, 0x37800000, v141
	v_cndmask_b32_e32 v141, v141, v142, vcc
	v_mov_b32_e32 v142, v137
	v_mov_b32_e32 v143, v138
	v_mov_b32_e32 v137, v139
	v_pk_add_f32 v[136:137], v[142:143], v[136:137]
	v_cmp_class_f32_e32 vcc, v140, v248
	v_add_f32_e32 v136, v136, v137
	ds_swizzle_b32 v137, v136 offset:swizzle(SWAP,16)
	v_cndmask_b32_e32 v140, v141, v140, vcc
	v_rcp_f32_e32 v140, v140
	s_waitcnt lgkmcnt(0)
	v_add_f32_e32 v136, v136, v137
	v_mov_b32_e32 v137, v136
	s_nop 1
	v_permlane32_swap_b32_e32 v136, v137
	v_add_f32_e32 v136, v136, v137
	v_fmamk_f32 v136, v136, 0x3a800000, v212
	v_cmp_gt_f32_e32 vcc, s2, v136
	v_mul_f32_e32 v137, 0x4f800000, v136
	s_nop 0
	v_cndmask_b32_e32 v136, v136, v137, vcc
	v_sqrt_f32_e32 v137, v136
	s_nop 0
	v_add_u32_e32 v138, -1, v137
	v_fma_f32 v139, -v138, v137, v136
	v_cmp_ge_f32_e64 s[4:5], 0, v139
	v_add_u32_e32 v139, 1, v137
	s_nop 0
	v_cndmask_b32_e64 v138, v137, v138, s[4:5]
	v_fma_f32 v137, -v139, v137, v136
	v_cmp_lt_f32_e64 s[4:5], 0, v137
	s_nop 1
	v_cndmask_b32_e64 v137, v138, v139, s[4:5]
	v_mul_f32_e32 v138, 0x37800000, v137
	v_cndmask_b32_e32 v137, v137, v138, vcc
	v_mov_b32_e32 v138, v133
	v_mov_b32_e32 v139, v134
	v_mov_b32_e32 v133, v135
	v_pk_add_f32 v[132:133], v[138:139], v[132:133]
	v_cmp_class_f32_e32 vcc, v136, v248
	v_add_f32_e32 v132, v132, v133
	ds_swizzle_b32 v133, v132 offset:swizzle(SWAP,16)
	v_cndmask_b32_e32 v136, v137, v136, vcc
	v_rcp_f32_e32 v136, v136
	s_waitcnt lgkmcnt(0)
	v_add_f32_e32 v132, v132, v133
	v_mov_b32_e32 v133, v132
	s_nop 1
	v_permlane32_swap_b32_e32 v132, v133
	v_add_f32_e32 v132, v132, v133
	v_fmamk_f32 v132, v132, 0x3a800000, v212
	v_cmp_gt_f32_e32 vcc, s2, v132
	v_mul_f32_e32 v133, 0x4f800000, v132
	s_nop 0
	v_cndmask_b32_e32 v132, v132, v133, vcc
	v_sqrt_f32_e32 v133, v132
	s_nop 0
	v_add_u32_e32 v134, -1, v133
	v_fma_f32 v135, -v134, v133, v132
	v_cmp_ge_f32_e64 s[4:5], 0, v135
	v_add_u32_e32 v135, 1, v133
	s_nop 0
	v_cndmask_b32_e64 v134, v133, v134, s[4:5]
	v_fma_f32 v133, -v135, v133, v132
	v_cmp_lt_f32_e64 s[4:5], 0, v133
	s_nop 1
	v_cndmask_b32_e64 v133, v134, v135, s[4:5]
	v_mul_f32_e32 v134, 0x37800000, v133
	v_cndmask_b32_e32 v133, v133, v134, vcc
	v_mov_b32_e32 v134, v129
	v_mov_b32_e32 v135, v130
	v_mov_b32_e32 v129, v131
	v_pk_add_f32 v[128:129], v[134:135], v[128:129]
	v_cmp_class_f32_e32 vcc, v132, v248
	v_add_f32_e32 v128, v128, v129
	ds_swizzle_b32 v129, v128 offset:swizzle(SWAP,16)
	v_cndmask_b32_e32 v132, v133, v132, vcc
	v_rcp_f32_e32 v132, v132
	s_waitcnt lgkmcnt(0)
; __device__ __forceinline__ float rcpf_(float x) { float r = __builtin_amdgcn_rcpf(x); asm volatile("s_nop 0" : "+v"(r)); return r; }
; __device__ __forceinline__ float sigmoidf_(float x) { return rcpf_(1.0f + __expf(-x)); }
;     __device__ __forceinline__ bool operator()(f32x4 (&acc)[2][2][4][2], const pg8::Unit& u, int wr, int wc, int fr, int fq) const {
;     ...
;         for (int ai = 0; ai < 2; ++ai)
; #pragma unroll
;             for (int m = 0; m < 4; ++m) { const int rl = ai * 128 + wr * 64 + m * 16 + fr; const float s = rs_[ai][m];
;                 f32x4 o[2];
; #pragma unroll
;                 for (int n = 0; n < 2; ++n) { const f32x4 g = acc[ai][0][m][n] * s, up = acc[ai][1][m][n] * s;
; #pragma unroll
;                     for (int j = 0; j < 4; ++j) o[n][j] = g[j] * sigmoidf_(g[j]) * up[j]; }
;                 st8_wt(ACT + (size_t)(u.pm * 256 + rl) * DE + colb, o[0], o[1]); }
	v_add_f32_e32 v128, v128, v129
	v_mov_b32_e32 v129, v128
	s_nop 1
	v_permlane32_swap_b32_e32 v128, v129
	v_add_f32_e32 v128, v128, v129
	v_fmamk_f32 v128, v128, 0x3a800000, v212
	v_cmp_gt_f32_e32 vcc, s2, v128
	v_mul_f32_e32 v129, 0x4f800000, v128
	v_readlane_b32 s2, v251, 54
	v_cndmask_b32_e32 v128, v128, v129, vcc
	v_sqrt_f32_e32 v129, v128
	v_readlane_b32 s3, v251, 55
	v_add_u32_e32 v130, -1, v129
	v_fma_f32 v131, -v130, v129, v128
	v_cmp_ge_f32_e64 s[4:5], 0, v131
	v_add_u32_e32 v131, 1, v129
	s_nop 0
	v_cndmask_b32_e64 v130, v129, v130, s[4:5]
	v_fma_f32 v129, -v131, v129, v128
	v_cmp_lt_f32_e64 s[4:5], 0, v129
	s_nop 1
	v_cndmask_b32_e64 v129, v130, v131, s[4:5]
	v_mul_f32_e32 v130, 0x37800000, v129
	v_cndmask_b32_e32 v129, v129, v130, vcc
	v_mov_b32_e32 v130, v68
	v_mov_b32_e32 v131, v104
	v_cmp_class_f32_e32 vcc, v128, v248
	v_pk_mul_f32 v[130:131], v[130:131], v[176:177] op_sel_hi:[1,0]
	s_lshl_b32 s4, s44, 8
	v_cndmask_b32_e32 v128, v129, v128, vcc
	v_mul_f32_e32 v129, 0xbfb8aa3b, v131
	v_exp_f32_e32 v129, v129
	s_movk_i32 s5, 0x600
	v_rcp_f32_e32 v128, v128
	v_add_f32_e32 v129, 1.0, v129
	v_rcp_f32_e32 v129, v129
	s_nop 0
	s_nop 0
	v_mul_f32_e32 v129, v131, v129
	v_mul_f32_e32 v129, v130, v129
	v_mov_b32_e32 v130, v69
	v_mov_b32_e32 v131, v105
	v_pk_mul_f32 v[130:131], v[130:131], v[176:177] op_sel_hi:[1,0]
	s_nop 0
	v_mul_f32_e32 v133, 0xbfb8aa3b, v131
	v_exp_f32_e32 v133, v133
	s_nop 0
	v_add_f32_e32 v133, 1.0, v133
	v_rcp_f32_e32 v133, v133
	s_nop 0
	s_nop 0
	v_mul_f32_e32 v131, v131, v133
	v_mul_f32_e32 v133, v130, v131
	v_mov_b32_e32 v130, v70
	v_mov_b32_e32 v131, v106
	v_pk_mul_f32 v[130:131], v[130:131], v[176:177] op_sel_hi:[1,0]
	s_nop 0
	v_mul_f32_e32 v134, 0xbfb8aa3b, v131
	v_exp_f32_e32 v134, v134
	s_nop 0
	v_add_f32_e32 v134, 1.0, v134
	v_rcp_f32_e32 v134, v134
	s_nop 0
	s_nop 0
	v_mul_f32_e32 v131, v131, v134
	v_mul_f32_e32 v137, v130, v131
	v_mov_b32_e32 v130, v71
	v_mov_b32_e32 v131, v107
	v_pk_mul_f32 v[130:131], v[130:131], v[176:177] op_sel_hi:[1,0]
	s_nop 0
	v_mul_f32_e32 v134, 0xbfb8aa3b, v131
	v_exp_f32_e32 v134, v134
	s_nop 0
	v_add_f32_e32 v134, 1.0, v134
	v_rcp_f32_e32 v134, v134
	s_nop 0
	s_nop 0
	v_mul_f32_e32 v131, v131, v134
	v_mul_f32_e32 v141, v130, v131
	v_mov_b32_e32 v130, v64
	v_mov_b32_e32 v131, v96
	v_pk_mul_f32 v[130:131], v[130:131], v[176:177] op_sel_hi:[1,0]
	s_nop 0
	v_mul_f32_e32 v134, 0xbfb8aa3b, v131
	v_exp_f32_e32 v134, v134
	s_nop 0
	v_add_f32_e32 v134, 1.0, v134
	v_rcp_f32_e32 v134, v134
	s_nop 0
	s_nop 0
	v_mul_f32_e32 v131, v131, v134
	v_mul_f32_e32 v142, v130, v131
	v_mov_b32_e32 v130, v65
	v_mov_b32_e32 v131, v97
	v_pk_mul_f32 v[130:131], v[130:131], v[176:177] op_sel_hi:[1,0]
	s_nop 0
	v_mul_f32_e32 v134, 0xbfb8aa3b, v131
	v_exp_f32_e32 v134, v134
	s_nop 0
	v_add_f32_e32 v134, 1.0, v134
	v_rcp_f32_e32 v134, v134
	s_nop 0
	s_nop 0
	v_mul_f32_e32 v131, v131, v134
	v_mul_f32_e32 v143, v130, v131
	v_mov_b32_e32 v130, v66
	v_mov_b32_e32 v131, v98
	v_pk_mul_f32 v[130:131], v[130:131], v[176:177] op_sel_hi:[1,0]
	s_nop 0
	v_mul_f32_e32 v134, 0xbfb8aa3b, v131
	v_exp_f32_e32 v134, v134
	s_nop 0
	v_add_f32_e32 v134, 1.0, v134
	v_rcp_f32_e32 v134, v134
	s_nop 0
	s_nop 0
	v_mul_f32_e32 v131, v131, v134
	v_mul_f32_e32 v145, v130, v131
	v_mov_b32_e32 v130, v67
	v_mov_b32_e32 v131, v99
	v_pk_mul_f32 v[130:131], v[130:131], v[176:177] op_sel_hi:[1,0]
	s_nop 0
	v_mul_f32_e32 v134, 0xbfb8aa3b, v131
	v_exp_f32_e32 v134, v134
	s_nop 0
	v_add_f32_e32 v134, 1.0, v134
	v_rcp_f32_e32 v134, v134
	s_nop 0
	s_nop 0
	v_mul_f32_e32 v131, v131, v134
	v_mul_f32_e32 v146, v130, v131
	v_add_u32_e32 v134, s4, v162
	v_mov_b64_e32 v[130:131], s[2:3]
	v_mad_i64_i32 v[138:139], s[2:3], v134, s5, v[130:131]
	v_lshlrev_b64 v[134:135], 1, v[174:175]
	v_lshl_add_u64 v[138:139], v[138:139], 0, v[134:135]
	v_cvt_pk_bf16_f32 v174, v129, v133
	v_cvt_pk_bf16_f32 v175, v137, v141
	v_cvt_pk_bf16_f32 v176, v142, v143
	v_cvt_pk_bf16_f32 v177, v145, v146
	s_nop 0
	global_store_dwordx4 v[138:139], v[174:177], off sc1
	s_nop 1
	v_mov_b32_e32 v138, v60
	v_mov_b32_e32 v139, v92
	v_pk_mul_f32 v[138:139], v[138:139], v[160:161] op_sel_hi:[1,0]
	s_nop 0
	v_mul_f32_e32 v129, 0xbfb8aa3b, v139
	v_exp_f32_e32 v129, v129
	s_nop 0
	v_add_f32_e32 v129, 1.0, v129
	v_rcp_f32_e32 v129, v129
	s_nop 0
	s_nop 0
	v_mul_f32_e32 v129, v139, v129
	v_mul_f32_e32 v129, v138, v129
	v_mov_b32_e32 v138, v61
	v_mov_b32_e32 v139, v93
	v_pk_mul_f32 v[138:139], v[138:139], v[160:161] op_sel_hi:[1,0]
	s_nop 0
	v_mul_f32_e32 v133, 0xbfb8aa3b, v139
	v_exp_f32_e32 v133, v133
	s_nop 0
	v_add_f32_e32 v133, 1.0, v133
	v_rcp_f32_e32 v133, v133
	s_nop 0
	s_nop 0
	v_mul_f32_e32 v133, v139, v133
	v_mul_f32_e32 v133, v138, v133
	v_mov_b32_e32 v138, v62
	v_mov_b32_e32 v139, v94
	v_pk_mul_f32 v[138:139], v[138:139], v[160:161] op_sel_hi:[1,0]
	s_nop 0
	v_mul_f32_e32 v137, 0xbfb8aa3b, v139
	v_exp_f32_e32 v137, v137
	s_nop 0
	v_add_f32_e32 v137, 1.0, v137
	v_rcp_f32_e32 v137, v137
	s_nop 0
	s_nop 0
	v_mul_f32_e32 v137, v139, v137
	v_mul_f32_e32 v137, v138, v137
	v_mov_b32_e32 v138, v63
	v_mov_b32_e32 v139, v95
	v_pk_mul_f32 v[138:139], v[138:139], v[160:161] op_sel_hi:[1,0]
	s_nop 0
	v_mul_f32_e32 v141, 0xbfb8aa3b, v139
	v_exp_f32_e32 v141, v141
	s_nop 0
	v_add_f32_e32 v141, 1.0, v141
	v_rcp_f32_e32 v141, v141
	s_nop 0
	s_nop 0
	v_mul_f32_e32 v139, v139, v141
	v_mul_f32_e32 v141, v138, v139
	v_mov_b32_e32 v138, v56
	v_mov_b32_e32 v139, v88
	v_pk_mul_f32 v[138:139], v[138:139], v[160:161] op_sel_hi:[1,0]
	s_nop 0
	v_mul_f32_e32 v142, 0xbfb8aa3b, v139
	v_exp_f32_e32 v142, v142
	s_nop 0
	v_add_f32_e32 v142, 1.0, v142
	v_rcp_f32_e32 v142, v142
	s_nop 0
	s_nop 0
; __device__ __forceinline__ float sigmoidf_(float x) { return rcpf_(1.0f + __expf(-x)); }
;     __device__ __forceinline__ bool operator()(f32x4 (&acc)[2][2][4][2], const pg8::Unit& u, int wr, int wc, int fr, int fq) const {
;     ...
;         for (int ai = 0; ai < 2; ++ai)
; #pragma unroll
;             for (int m = 0; m < 4; ++m) { const int rl = ai * 128 + wr * 64 + m * 16 + fr; const float s = rs_[ai][m];
;                 f32x4 o[2];
; #pragma unroll
;                 for (int n = 0; n < 2; ++n) { const f32x4 g = acc[ai][0][m][n] * s, up = acc[ai][1][m][n] * s;
; #pragma unroll
;                     for (int j = 0; j < 4; ++j) o[n][j] = g[j] * sigmoidf_(g[j]) * up[j]; }
;                 st8_wt(ACT + (size_t)(u.pm * 256 + rl) * DE + colb, o[0], o[1]); }
	v_mul_f32_e32 v139, v139, v142
	v_mul_f32_e32 v142, v138, v139
	v_mov_b32_e32 v138, v57
	v_mov_b32_e32 v139, v89
	v_pk_mul_f32 v[138:139], v[138:139], v[160:161] op_sel_hi:[1,0]
	s_nop 0
	v_mul_f32_e32 v143, 0xbfb8aa3b, v139
	v_exp_f32_e32 v143, v143
	s_nop 0
	v_add_f32_e32 v143, 1.0, v143
	v_rcp_f32_e32 v143, v143
	s_nop 0
	s_nop 0
	v_mul_f32_e32 v139, v139, v143
	v_mul_f32_e32 v143, v138, v139
	v_mov_b32_e32 v138, v58
	v_mov_b32_e32 v139, v90
	v_pk_mul_f32 v[138:139], v[138:139], v[160:161] op_sel_hi:[1,0]
	s_nop 0
	v_mul_f32_e32 v145, 0xbfb8aa3b, v139
	v_exp_f32_e32 v145, v145
	s_nop 0
	v_add_f32_e32 v145, 1.0, v145
	v_rcp_f32_e32 v145, v145
	s_nop 0
	s_nop 0
	v_mul_f32_e32 v139, v139, v145
	v_mul_f32_e32 v145, v138, v139
	v_mov_b32_e32 v138, v59
	v_mov_b32_e32 v139, v91
	v_pk_mul_f32 v[138:139], v[138:139], v[160:161] op_sel_hi:[1,0]
	s_nop 0
	v_mul_f32_e32 v146, 0xbfb8aa3b, v139
	v_exp_f32_e32 v146, v146
	s_nop 0
	v_add_f32_e32 v146, 1.0, v146
	v_rcp_f32_e32 v146, v146
	s_nop 0
	v_cvt_pk_bf16_f32 v174, v129, v133
	v_cvt_pk_bf16_f32 v175, v137, v141
	v_cvt_pk_bf16_f32 v176, v142, v143
	s_nop 0
	v_mul_f32_e32 v139, v139, v146
	v_mul_f32_e32 v146, v138, v139
	v_add_u32_e32 v138, s4, v171
	v_mad_i64_i32 v[138:139], s[2:3], v138, s5, v[130:131]
	v_lshl_add_u64 v[138:139], v[138:139], 0, v[134:135]
	v_cvt_pk_bf16_f32 v177, v145, v146
	s_nop 0
	global_store_dwordx4 v[138:139], v[174:177], off sc1
	s_nop 1
	v_mov_b32_e32 v138, v52
	v_mov_b32_e32 v139, v84
	v_pk_mul_f32 v[138:139], v[138:139], v[148:149] op_sel_hi:[1,0]
	s_nop 0
	v_mul_f32_e32 v129, 0xbfb8aa3b, v139
	v_exp_f32_e32 v129, v129
	s_nop 0
	v_add_f32_e32 v129, 1.0, v129
	v_rcp_f32_e32 v129, v129
	s_nop 0
	s_nop 0
	v_mul_f32_e32 v129, v139, v129
	v_mul_f32_e32 v129, v138, v129
	v_mov_b32_e32 v138, v53
	v_mov_b32_e32 v139, v85
	v_pk_mul_f32 v[138:139], v[138:139], v[148:149] op_sel_hi:[1,0]
	s_nop 0
	v_mul_f32_e32 v133, 0xbfb8aa3b, v139
	v_exp_f32_e32 v133, v133
	s_nop 0
	v_add_f32_e32 v133, 1.0, v133
	v_rcp_f32_e32 v133, v133
	s_nop 0
	s_nop 0
	v_mul_f32_e32 v133, v139, v133
	v_mul_f32_e32 v133, v138, v133
	v_mov_b32_e32 v138, v54
	v_mov_b32_e32 v139, v86
	v_pk_mul_f32 v[138:139], v[138:139], v[148:149] op_sel_hi:[1,0]
	s_nop 0
	v_mul_f32_e32 v137, 0xbfb8aa3b, v139
	v_exp_f32_e32 v137, v137
	s_nop 0
	v_add_f32_e32 v137, 1.0, v137
	v_rcp_f32_e32 v137, v137
	s_nop 0
	s_nop 0
	v_mul_f32_e32 v137, v139, v137
	v_mul_f32_e32 v137, v138, v137
	v_mov_b32_e32 v138, v55
	v_mov_b32_e32 v139, v87
	v_pk_mul_f32 v[138:139], v[138:139], v[148:149] op_sel_hi:[1,0]
	s_nop 0
	v_mul_f32_e32 v141, 0xbfb8aa3b, v139
	v_exp_f32_e32 v141, v141
	s_nop 0
	v_add_f32_e32 v141, 1.0, v141
	v_rcp_f32_e32 v141, v141
	s_nop 0
	s_nop 0
	v_mul_f32_e32 v139, v139, v141
	v_mul_f32_e32 v141, v138, v139
	v_mov_b32_e32 v138, v48
	v_mov_b32_e32 v139, v80
	v_pk_mul_f32 v[138:139], v[138:139], v[148:149] op_sel_hi:[1,0]
	s_nop 0
	v_mul_f32_e32 v142, 0xbfb8aa3b, v139
	v_exp_f32_e32 v142, v142
	s_nop 0
	v_add_f32_e32 v142, 1.0, v142
	v_rcp_f32_e32 v142, v142
	s_nop 0
	s_nop 0
	v_mul_f32_e32 v139, v139, v142
	v_mul_f32_e32 v142, v138, v139
	v_mov_b32_e32 v138, v49
	v_mov_b32_e32 v139, v81
	v_pk_mul_f32 v[138:139], v[138:139], v[148:149] op_sel_hi:[1,0]
	s_nop 0
	v_mul_f32_e32 v143, 0xbfb8aa3b, v139
	v_exp_f32_e32 v143, v143
	s_nop 0
	v_add_f32_e32 v143, 1.0, v143
	v_rcp_f32_e32 v143, v143
	s_nop 0
	s_nop 0
	v_mul_f32_e32 v139, v139, v143
	v_mul_f32_e32 v143, v138, v139
	v_mov_b32_e32 v138, v50
	v_mov_b32_e32 v139, v82
	v_pk_mul_f32 v[138:139], v[138:139], v[148:149] op_sel_hi:[1,0]
	s_nop 0
	v_mul_f32_e32 v145, 0xbfb8aa3b, v139
	v_exp_f32_e32 v145, v145
	s_nop 0
	v_add_f32_e32 v145, 1.0, v145
	v_rcp_f32_e32 v145, v145
	s_nop 0
	s_nop 0
	v_mul_f32_e32 v139, v139, v145
	v_mul_f32_e32 v145, v138, v139
	v_mov_b32_e32 v138, v51
	v_mov_b32_e32 v139, v83
	v_pk_mul_f32 v[138:139], v[138:139], v[148:149] op_sel_hi:[1,0]
	s_nop 0
	v_mul_f32_e32 v146, 0xbfb8aa3b, v139
	v_exp_f32_e32 v146, v146
	s_nop 0
	v_add_f32_e32 v146, 1.0, v146
	v_rcp_f32_e32 v146, v146
	s_nop 0
	s_nop 0
	v_mul_f32_e32 v139, v139, v146
	v_mul_f32_e32 v149, v138, v139
	v_add_u32_e32 v138, s4, v183
	v_mad_i64_i32 v[138:139], s[2:3], v138, s5, v[130:131]
	v_lshl_add_u64 v[138:139], v[138:139], 0, v[134:135]
	v_cvt_pk_bf16_f32 v146, v129, v133
	v_cvt_pk_bf16_f32 v147, v137, v141
	v_cvt_pk_bf16_f32 v148, v142, v143
	v_cvt_pk_bf16_f32 v149, v145, v149
	s_nop 0
	global_store_dwordx4 v[138:139], v[146:149], off sc1
	s_nop 1
	v_mov_b32_e32 v138, v44
	v_mov_b32_e32 v139, v76
	v_pk_mul_f32 v[138:139], v[138:139], v[144:145] op_sel_hi:[1,0]
	s_nop 0
	v_mul_f32_e32 v129, 0xbfb8aa3b, v139
	v_exp_f32_e32 v129, v129
	s_nop 0
	v_add_f32_e32 v129, 1.0, v129
	v_rcp_f32_e32 v129, v129
	s_nop 0
	s_nop 0
	v_mul_f32_e32 v129, v139, v129
	v_mul_f32_e32 v129, v138, v129
	v_mov_b32_e32 v138, v45
	v_mov_b32_e32 v139, v77
	v_pk_mul_f32 v[138:139], v[138:139], v[144:145] op_sel_hi:[1,0]
	s_nop 0
	v_mul_f32_e32 v133, 0xbfb8aa3b, v139
	v_exp_f32_e32 v133, v133
	s_nop 0
	v_add_f32_e32 v133, 1.0, v133
	v_rcp_f32_e32 v133, v133
	s_nop 0
	s_nop 0
	v_mul_f32_e32 v133, v139, v133
	v_mul_f32_e32 v133, v138, v133
	v_mov_b32_e32 v138, v46
	v_mov_b32_e32 v139, v78
	v_pk_mul_f32 v[138:139], v[138:139], v[144:145] op_sel_hi:[1,0]
	s_nop 0
	v_mul_f32_e32 v137, 0xbfb8aa3b, v139
	v_exp_f32_e32 v137, v137
	s_nop 0
	v_add_f32_e32 v137, 1.0, v137
	v_rcp_f32_e32 v137, v137
	s_nop 0
	s_nop 0
	v_mul_f32_e32 v137, v139, v137
	v_mul_f32_e32 v137, v138, v137
	v_mov_b32_e32 v138, v47
	v_mov_b32_e32 v139, v79
	v_pk_mul_f32 v[138:139], v[138:139], v[144:145] op_sel_hi:[1,0]
	s_nop 0
	v_mul_f32_e32 v141, 0xbfb8aa3b, v139
; __device__ __forceinline__ float sigmoidf_(float x) { return rcpf_(1.0f + __expf(-x)); }
;     __device__ __forceinline__ bool operator()(f32x4 (&acc)[2][2][4][2], const pg8::Unit& u, int wr, int wc, int fr, int fq) const {
;     ...
;         for (int ai = 0; ai < 2; ++ai)
; #pragma unroll
;             for (int m = 0; m < 4; ++m) { const int rl = ai * 128 + wr * 64 + m * 16 + fr; const float s = rs_[ai][m];
;                 f32x4 o[2];
; #pragma unroll
;                 for (int n = 0; n < 2; ++n) { const f32x4 g = acc[ai][0][m][n] * s, up = acc[ai][1][m][n] * s;
; #pragma unroll
;                     for (int j = 0; j < 4; ++j) o[n][j] = g[j] * sigmoidf_(g[j]) * up[j]; }
;                 st8_wt(ACT + (size_t)(u.pm * 256 + rl) * DE + colb, o[0], o[1]); }
	v_exp_f32_e32 v141, v141
	s_nop 0
	v_add_f32_e32 v141, 1.0, v141
	v_rcp_f32_e32 v141, v141
	s_nop 0
	s_nop 0
	v_mul_f32_e32 v139, v139, v141
	v_mul_f32_e32 v141, v138, v139
	v_mov_b32_e32 v138, v40
	v_mov_b32_e32 v139, v72
	v_pk_mul_f32 v[138:139], v[138:139], v[144:145] op_sel_hi:[1,0]
	s_nop 0
	v_mul_f32_e32 v142, 0xbfb8aa3b, v139
	v_exp_f32_e32 v142, v142
	s_nop 0
	v_add_f32_e32 v142, 1.0, v142
	v_rcp_f32_e32 v142, v142
	s_nop 0
	s_nop 0
	v_mul_f32_e32 v139, v139, v142
	v_mul_f32_e32 v145, v138, v139
	v_mov_b32_e32 v138, v41
	v_mov_b32_e32 v139, v73
	v_pk_mul_f32 v[138:139], v[138:139], v[144:145] op_sel_hi:[1,0]
	s_nop 0
	v_mul_f32_e32 v142, 0xbfb8aa3b, v139
	v_exp_f32_e32 v142, v142
	s_nop 0
	v_add_f32_e32 v142, 1.0, v142
	v_rcp_f32_e32 v142, v142
	s_nop 0
	s_nop 0
	v_mul_f32_e32 v139, v139, v142
	v_mul_f32_e32 v146, v138, v139
	v_mov_b32_e32 v138, v42
	v_mov_b32_e32 v139, v74
	v_pk_mul_f32 v[138:139], v[138:139], v[144:145] op_sel_hi:[1,0]
	s_nop 0
	v_mul_f32_e32 v142, 0xbfb8aa3b, v139
	v_exp_f32_e32 v142, v142
	s_nop 0
	v_add_f32_e32 v142, 1.0, v142
	v_rcp_f32_e32 v142, v142
	s_nop 0
	s_nop 0
	v_mul_f32_e32 v139, v139, v142
	v_mul_f32_e32 v147, v138, v139
	v_mov_b32_e32 v138, v43
	v_mov_b32_e32 v139, v75
	v_pk_mul_f32 v[138:139], v[138:139], v[144:145] op_sel_hi:[1,0]
	s_nop 0
	v_mul_f32_e32 v142, 0xbfb8aa3b, v139
	v_exp_f32_e32 v142, v142
	s_nop 0
	v_add_f32_e32 v142, 1.0, v142
	v_rcp_f32_e32 v142, v142
	s_nop 0
	s_nop 0
	v_mul_f32_e32 v139, v139, v142
	v_mul_f32_e32 v148, v138, v139
	v_add_u32_e32 v138, s4, v201
	v_mad_i64_i32 v[138:139], s[2:3], v138, s5, v[130:131]
	v_lshl_add_u64 v[138:139], v[138:139], 0, v[134:135]
	v_cvt_pk_bf16_f32 v142, v129, v133
	v_cvt_pk_bf16_f32 v143, v137, v141
	v_cvt_pk_bf16_f32 v144, v145, v146
	v_cvt_pk_bf16_f32 v145, v147, v148
	s_nop 0
	global_store_dwordx4 v[138:139], v[142:145], off sc1
	s_nop 1
	v_mov_b32_e32 v138, v4
	v_mov_b32_e32 v139, v36
	v_pk_mul_f32 v[138:139], v[138:139], v[140:141] op_sel_hi:[1,0]
	s_nop 0
	v_mul_f32_e32 v129, 0xbfb8aa3b, v139
	v_exp_f32_e32 v129, v129
	s_nop 0
	v_add_f32_e32 v129, 1.0, v129
	v_rcp_f32_e32 v129, v129
	s_nop 0
	s_nop 0
	v_mul_f32_e32 v129, v139, v129
	v_mul_f32_e32 v129, v138, v129
	v_mov_b32_e32 v138, v5
	v_mov_b32_e32 v139, v37
	v_pk_mul_f32 v[138:139], v[138:139], v[140:141] op_sel_hi:[1,0]
	s_nop 0
	v_mul_f32_e32 v133, 0xbfb8aa3b, v139
	v_exp_f32_e32 v133, v133
	s_nop 0
	v_add_f32_e32 v133, 1.0, v133
	v_rcp_f32_e32 v133, v133
	s_nop 0
	s_nop 0
	v_mul_f32_e32 v133, v139, v133
	v_mul_f32_e32 v133, v138, v133
	v_mov_b32_e32 v138, v6
	v_mov_b32_e32 v139, v38
	v_pk_mul_f32 v[138:139], v[138:139], v[140:141] op_sel_hi:[1,0]
	s_nop 0
	v_mul_f32_e32 v137, 0xbfb8aa3b, v139
	v_exp_f32_e32 v137, v137
	s_nop 0
	v_add_f32_e32 v137, 1.0, v137
	v_rcp_f32_e32 v137, v137
	s_nop 0
	s_nop 0
	v_mul_f32_e32 v137, v139, v137
	v_mul_f32_e32 v137, v138, v137
	v_mov_b32_e32 v138, v7
	v_mov_b32_e32 v139, v39
	v_pk_mul_f32 v[138:139], v[138:139], v[140:141] op_sel_hi:[1,0]
	s_nop 0
	v_mul_f32_e32 v141, 0xbfb8aa3b, v139
	v_exp_f32_e32 v141, v141
	s_nop 0
	v_add_f32_e32 v141, 1.0, v141
	v_rcp_f32_e32 v141, v141
	s_nop 0
	s_nop 0
	v_mul_f32_e32 v139, v139, v141
	v_mul_f32_e32 v141, v138, v139
	v_mov_b32_e32 v138, v0
	v_mov_b32_e32 v139, v32
	v_pk_mul_f32 v[138:139], v[138:139], v[140:141] op_sel_hi:[1,0]
	s_nop 0
	v_mul_f32_e32 v142, 0xbfb8aa3b, v139
	v_exp_f32_e32 v142, v142
	s_nop 0
	v_add_f32_e32 v142, 1.0, v142
	v_rcp_f32_e32 v142, v142
	s_nop 0
	s_nop 0
	v_mul_f32_e32 v139, v139, v142
	v_mul_f32_e32 v144, v138, v139
	v_mov_b32_e32 v138, v1
	v_mov_b32_e32 v139, v33
	v_pk_mul_f32 v[138:139], v[138:139], v[140:141] op_sel_hi:[1,0]
	s_nop 0
	v_mul_f32_e32 v142, 0xbfb8aa3b, v139
	v_exp_f32_e32 v142, v142
	s_nop 0
	v_add_f32_e32 v142, 1.0, v142
	v_rcp_f32_e32 v142, v142
	s_nop 0
	s_nop 0
	v_mul_f32_e32 v139, v139, v142
	v_mul_f32_e32 v145, v138, v139
	v_mov_b32_e32 v138, v2
	v_mov_b32_e32 v139, v34
	v_pk_mul_f32 v[138:139], v[138:139], v[140:141] op_sel_hi:[1,0]
	s_nop 0
	v_mul_f32_e32 v142, 0xbfb8aa3b, v139
	v_exp_f32_e32 v142, v142
	s_nop 0
	v_add_f32_e32 v142, 1.0, v142
	v_rcp_f32_e32 v142, v142
	s_nop 0
	s_nop 0
	v_mul_f32_e32 v139, v139, v142
	v_mul_f32_e32 v146, v138, v139
	v_mov_b32_e32 v138, v3
	v_mov_b32_e32 v139, v35
	v_pk_mul_f32 v[138:139], v[138:139], v[140:141] op_sel_hi:[1,0]
	s_nop 0
	v_mul_f32_e32 v140, 0xbfb8aa3b, v139
	v_exp_f32_e32 v140, v140
	s_nop 0
	v_add_f32_e32 v140, 1.0, v140
	v_rcp_f32_e32 v140, v140
	s_nop 0
	s_nop 0
	v_mul_f32_e32 v139, v139, v140
	v_mul_f32_e32 v147, v138, v139
	v_add_u32_e32 v138, s4, v213
	v_mad_i64_i32 v[138:139], s[2:3], v138, s5, v[130:131]
	v_lshl_add_u64 v[142:143], v[138:139], 0, v[134:135]
	v_cvt_pk_bf16_f32 v138, v129, v133
	v_cvt_pk_bf16_f32 v139, v137, v141
	v_cvt_pk_bf16_f32 v140, v144, v145
	v_cvt_pk_bf16_f32 v141, v146, v147
	s_nop 0
	global_store_dwordx4 v[142:143], v[138:141], off sc1
	s_nop 1
	v_mov_b32_e32 v138, v100
	v_mov_b32_e32 v139, v28
	v_pk_mul_f32 v[138:139], v[138:139], v[136:137] op_sel_hi:[1,0]
	s_nop 0
	v_mul_f32_e32 v129, 0xbfb8aa3b, v139
	v_exp_f32_e32 v129, v129
	s_nop 0
	v_add_f32_e32 v129, 1.0, v129
	v_rcp_f32_e32 v129, v129
	s_nop 0
	s_nop 0
	v_mul_f32_e32 v129, v139, v129
	v_mul_f32_e32 v129, v138, v129
	v_mov_b32_e32 v138, v101
	v_mov_b32_e32 v139, v29
	v_pk_mul_f32 v[138:139], v[138:139], v[136:137] op_sel_hi:[1,0]
	s_nop 0
	v_mul_f32_e32 v133, 0xbfb8aa3b, v139
	v_exp_f32_e32 v133, v133
	s_nop 0
	v_add_f32_e32 v133, 1.0, v133
	v_rcp_f32_e32 v133, v133
	s_nop 0
	s_nop 0
	v_mul_f32_e32 v133, v139, v133
	v_mul_f32_e32 v133, v138, v133
	v_mov_b32_e32 v138, v102
	v_mov_b32_e32 v139, v30
; __device__ __forceinline__ float sigmoidf_(float x) { return rcpf_(1.0f + __expf(-x)); }
;     __device__ __forceinline__ bool operator()(f32x4 (&acc)[2][2][4][2], const pg8::Unit& u, int wr, int wc, int fr, int fq) const {
;     ...
;         for (int ai = 0; ai < 2; ++ai)
; #pragma unroll
;             for (int m = 0; m < 4; ++m) { const int rl = ai * 128 + wr * 64 + m * 16 + fr; const float s = rs_[ai][m];
;                 f32x4 o[2];
; #pragma unroll
;                 for (int n = 0; n < 2; ++n) { const f32x4 g = acc[ai][0][m][n] * s, up = acc[ai][1][m][n] * s;
; #pragma unroll
;                     for (int j = 0; j < 4; ++j) o[n][j] = g[j] * sigmoidf_(g[j]) * up[j]; }
;                 st8_wt(ACT + (size_t)(u.pm * 256 + rl) * DE + colb, o[0], o[1]); }
	v_pk_mul_f32 v[138:139], v[138:139], v[136:137] op_sel_hi:[1,0]
	s_nop 0
	v_mul_f32_e32 v137, 0xbfb8aa3b, v139
	v_exp_f32_e32 v137, v137
	s_nop 0
	v_add_f32_e32 v137, 1.0, v137
	v_rcp_f32_e32 v137, v137
	s_nop 0
	s_nop 0
	v_mul_f32_e32 v137, v139, v137
	v_mul_f32_e32 v142, v138, v137
	v_mov_b32_e32 v138, v103
	v_mov_b32_e32 v139, v31
	v_pk_mul_f32 v[138:139], v[138:139], v[136:137] op_sel_hi:[1,0]
	s_nop 0
	v_mul_f32_e32 v137, 0xbfb8aa3b, v139
	v_exp_f32_e32 v137, v137
	s_nop 0
	v_add_f32_e32 v137, 1.0, v137
	v_rcp_f32_e32 v137, v137
	s_nop 0
	s_nop 0
	v_mul_f32_e32 v137, v139, v137
	v_mul_f32_e32 v143, v138, v137
	v_mov_b32_e32 v138, v108
	v_mov_b32_e32 v139, v24
	v_pk_mul_f32 v[138:139], v[138:139], v[136:137] op_sel_hi:[1,0]
	s_nop 0
	v_mul_f32_e32 v137, 0xbfb8aa3b, v139
	v_exp_f32_e32 v137, v137
	s_nop 0
	v_add_f32_e32 v137, 1.0, v137
	v_rcp_f32_e32 v137, v137
	s_nop 0
	s_nop 0
	v_mul_f32_e32 v137, v139, v137
	v_mul_f32_e32 v144, v138, v137
	v_mov_b32_e32 v138, v109
	v_mov_b32_e32 v139, v25
	v_pk_mul_f32 v[138:139], v[138:139], v[136:137] op_sel_hi:[1,0]
	s_nop 0
	v_mul_f32_e32 v137, 0xbfb8aa3b, v139
	v_exp_f32_e32 v137, v137
	s_nop 0
	v_add_f32_e32 v137, 1.0, v137
	v_rcp_f32_e32 v137, v137
	s_nop 0
	s_nop 0
	v_mul_f32_e32 v137, v139, v137
	v_mul_f32_e32 v145, v138, v137
	v_mov_b32_e32 v138, v110
	v_mov_b32_e32 v139, v26
	v_pk_mul_f32 v[138:139], v[138:139], v[136:137] op_sel_hi:[1,0]
	s_nop 0
	v_mul_f32_e32 v137, 0xbfb8aa3b, v139
	v_exp_f32_e32 v137, v137
	s_nop 0
	v_add_f32_e32 v137, 1.0, v137
	v_rcp_f32_e32 v137, v137
	s_nop 0
	s_nop 0
	v_mul_f32_e32 v137, v139, v137
	v_mul_f32_e32 v146, v138, v137
	v_mov_b32_e32 v138, v111
	v_mov_b32_e32 v139, v27
	v_pk_mul_f32 v[136:137], v[138:139], v[136:137] op_sel_hi:[1,0]
	s_nop 0
	v_mul_f32_e32 v138, 0xbfb8aa3b, v137
	v_exp_f32_e32 v138, v138
	s_nop 0
	v_add_f32_e32 v138, 1.0, v138
	v_rcp_f32_e32 v138, v138
	s_nop 0
	s_nop 0
	v_mul_f32_e32 v137, v137, v138
	v_mul_f32_e32 v139, v136, v137
	v_add_u32_e32 v136, s4, v186
	v_mad_i64_i32 v[136:137], s[2:3], v136, s5, v[130:131]
	v_lshl_add_u64 v[140:141], v[136:137], 0, v[134:135]
	v_cvt_pk_bf16_f32 v136, v129, v133
	v_cvt_pk_bf16_f32 v137, v142, v143
	v_cvt_pk_bf16_f32 v138, v144, v145
	v_cvt_pk_bf16_f32 v139, v146, v139
	s_nop 0
	global_store_dwordx4 v[140:141], v[136:139], off sc1
	s_nop 1
	v_mov_b32_e32 v136, v112
	v_mov_b32_e32 v137, v20
	v_pk_mul_f32 v[136:137], v[136:137], v[132:133] op_sel_hi:[1,0]
	s_nop 0
	v_mul_f32_e32 v129, 0xbfb8aa3b, v137
	v_exp_f32_e32 v129, v129
	s_nop 0
	v_add_f32_e32 v129, 1.0, v129
	v_rcp_f32_e32 v129, v129
	s_nop 0
	s_nop 0
	v_mul_f32_e32 v129, v137, v129
	v_mul_f32_e32 v129, v136, v129
	v_mov_b32_e32 v136, v113
	v_mov_b32_e32 v137, v21
	v_pk_mul_f32 v[136:137], v[136:137], v[132:133] op_sel_hi:[1,0]
	s_nop 0
	v_mul_f32_e32 v133, 0xbfb8aa3b, v137
	v_exp_f32_e32 v133, v133
	s_nop 0
	v_add_f32_e32 v133, 1.0, v133
	v_rcp_f32_e32 v133, v133
	s_nop 0
	s_nop 0
	v_mul_f32_e32 v133, v137, v133
	v_mul_f32_e32 v138, v136, v133
	v_mov_b32_e32 v136, v114
	v_mov_b32_e32 v137, v22
	v_pk_mul_f32 v[136:137], v[136:137], v[132:133] op_sel_hi:[1,0]
	s_nop 0
	v_mul_f32_e32 v133, 0xbfb8aa3b, v137
	v_exp_f32_e32 v133, v133
	s_nop 0
	v_add_f32_e32 v133, 1.0, v133
	v_rcp_f32_e32 v133, v133
	s_nop 0
	s_nop 0
	v_mul_f32_e32 v133, v137, v133
	v_mul_f32_e32 v139, v136, v133
	v_mov_b32_e32 v136, v115
	v_mov_b32_e32 v137, v23
	v_pk_mul_f32 v[136:137], v[136:137], v[132:133] op_sel_hi:[1,0]
	s_nop 0
	v_mul_f32_e32 v133, 0xbfb8aa3b, v137
	v_exp_f32_e32 v133, v133
	s_nop 0
	v_add_f32_e32 v133, 1.0, v133
	v_rcp_f32_e32 v133, v133
	s_nop 0
	s_nop 0
	v_mul_f32_e32 v133, v137, v133
	v_mul_f32_e32 v140, v136, v133
	v_mov_b32_e32 v136, v116
	v_mov_b32_e32 v137, v16
	v_pk_mul_f32 v[136:137], v[136:137], v[132:133] op_sel_hi:[1,0]
	s_nop 0
	v_mul_f32_e32 v133, 0xbfb8aa3b, v137
	v_exp_f32_e32 v133, v133
	s_nop 0
	v_add_f32_e32 v133, 1.0, v133
	v_rcp_f32_e32 v133, v133
	s_nop 0
	s_nop 0
	v_mul_f32_e32 v133, v137, v133
	v_mul_f32_e32 v141, v136, v133
	v_mov_b32_e32 v136, v117
	v_mov_b32_e32 v137, v17
	v_pk_mul_f32 v[136:137], v[136:137], v[132:133] op_sel_hi:[1,0]
	s_nop 0
	v_mul_f32_e32 v133, 0xbfb8aa3b, v137
	v_exp_f32_e32 v133, v133
	s_nop 0
	v_add_f32_e32 v133, 1.0, v133
	v_rcp_f32_e32 v133, v133
	s_nop 0
	s_nop 0
	v_mul_f32_e32 v133, v137, v133
	v_mul_f32_e32 v142, v136, v133
	v_mov_b32_e32 v136, v118
	v_mov_b32_e32 v137, v18
	v_pk_mul_f32 v[136:137], v[136:137], v[132:133] op_sel_hi:[1,0]
; __device__ __forceinline__ float sigmoidf_(float x) { return rcpf_(1.0f + __expf(-x)); }
;     __device__ __forceinline__ bool operator()(f32x4 (&acc)[2][2][4][2], const pg8::Unit& u, int wr, int wc, int fr, int fq) const {
;     ...
;         for (int ai = 0; ai < 2; ++ai)
; #pragma unroll
;             for (int m = 0; m < 4; ++m) { const int rl = ai * 128 + wr * 64 + m * 16 + fr; const float s = rs_[ai][m];
;                 f32x4 o[2];
; #pragma unroll
;                 for (int n = 0; n < 2; ++n) { const f32x4 g = acc[ai][0][m][n] * s, up = acc[ai][1][m][n] * s;
; #pragma unroll
;                     for (int j = 0; j < 4; ++j) o[n][j] = g[j] * sigmoidf_(g[j]) * up[j]; }
;                 st8_wt(ACT + (size_t)(u.pm * 256 + rl) * DE + colb, o[0], o[1]); }
;         asm volatile("s_waitcnt vmcnt(0)" ::: "memory");
;         if ((fr | fq) == 0) __hip_atomic_fetch_add(done + 64 * u.pm, 1u, __ATOMIC_RELAXED, __HIP_MEMORY_SCOPE_AGENT);
;         return false;
	s_nop 0
	v_mul_f32_e32 v133, 0xbfb8aa3b, v137
	v_exp_f32_e32 v133, v133
	s_nop 0
	v_add_f32_e32 v133, 1.0, v133
	v_rcp_f32_e32 v133, v133
	s_nop 0
	s_nop 0
	v_mul_f32_e32 v133, v137, v133
	v_mul_f32_e32 v143, v136, v133
	v_mov_b32_e32 v136, v119
	v_mov_b32_e32 v137, v19
	v_pk_mul_f32 v[132:133], v[136:137], v[132:133] op_sel_hi:[1,0]
	s_nop 0
	v_mul_f32_e32 v136, 0xbfb8aa3b, v133
	v_exp_f32_e32 v136, v136
	s_nop 0
	v_add_f32_e32 v136, 1.0, v136
	v_rcp_f32_e32 v136, v136
	s_nop 0
	s_nop 0
	v_mul_f32_e32 v133, v133, v136
	v_mul_f32_e32 v144, v132, v133
	v_add_u32_e32 v132, s4, v187
	v_mad_i64_i32 v[132:133], s[2:3], v132, s5, v[130:131]
	v_lshl_add_u64 v[132:133], v[132:133], 0, v[134:135]
	v_cvt_pk_bf16_f32 v136, v129, v138
	v_cvt_pk_bf16_f32 v137, v139, v140
	v_cvt_pk_bf16_f32 v138, v141, v142
	v_cvt_pk_bf16_f32 v139, v143, v144
	s_nop 0
	global_store_dwordx4 v[132:133], v[136:139], off sc1
	s_nop 1
	v_mov_b32_e32 v132, v120
	v_mov_b32_e32 v133, v12
	v_pk_mul_f32 v[132:133], v[132:133], v[128:129] op_sel_hi:[1,0]
	s_nop 0
	v_mul_f32_e32 v129, 0xbfb8aa3b, v133
	v_exp_f32_e32 v129, v129
	s_nop 0
	v_add_f32_e32 v129, 1.0, v129
	v_rcp_f32_e32 v129, v129
	s_nop 0
	s_nop 0
	v_mul_f32_e32 v129, v133, v129
	v_mul_f32_e32 v136, v132, v129
	v_mov_b32_e32 v132, v121
	v_mov_b32_e32 v133, v13
	v_pk_mul_f32 v[132:133], v[132:133], v[128:129] op_sel_hi:[1,0]
	s_nop 0
	v_mul_f32_e32 v129, 0xbfb8aa3b, v133
	v_exp_f32_e32 v129, v129
	s_nop 0
	v_add_f32_e32 v129, 1.0, v129
	v_rcp_f32_e32 v129, v129
	s_nop 0
	s_nop 0
	v_mul_f32_e32 v129, v133, v129
	v_mul_f32_e32 v137, v132, v129
	v_mov_b32_e32 v132, v122
	v_mov_b32_e32 v133, v14
	v_pk_mul_f32 v[132:133], v[132:133], v[128:129] op_sel_hi:[1,0]
	s_nop 0
	v_mul_f32_e32 v129, 0xbfb8aa3b, v133
	v_exp_f32_e32 v129, v129
	s_nop 0
	v_add_f32_e32 v129, 1.0, v129
	v_rcp_f32_e32 v129, v129
	s_nop 0
	s_nop 0
	v_mul_f32_e32 v129, v133, v129
	v_mul_f32_e32 v138, v132, v129
	v_mov_b32_e32 v132, v123
	v_mov_b32_e32 v133, v15
	v_pk_mul_f32 v[132:133], v[132:133], v[128:129] op_sel_hi:[1,0]
	s_nop 0
	v_mul_f32_e32 v129, 0xbfb8aa3b, v133
	v_exp_f32_e32 v129, v129
	s_nop 0
	v_add_f32_e32 v129, 1.0, v129
	v_rcp_f32_e32 v129, v129
	s_nop 0
	s_nop 0
	v_mul_f32_e32 v129, v133, v129
	v_mul_f32_e32 v139, v132, v129
	v_mov_b32_e32 v132, v124
	v_mov_b32_e32 v133, v8
	v_pk_mul_f32 v[132:133], v[132:133], v[128:129] op_sel_hi:[1,0]
	s_nop 0
	v_mul_f32_e32 v129, 0xbfb8aa3b, v133
	v_exp_f32_e32 v129, v129
	s_nop 0
	v_add_f32_e32 v129, 1.0, v129
	v_rcp_f32_e32 v129, v129
	s_nop 0
	s_nop 0
	v_mul_f32_e32 v129, v133, v129
	v_mul_f32_e32 v140, v132, v129
	v_mov_b32_e32 v132, v125
	v_mov_b32_e32 v133, v9
	v_pk_mul_f32 v[132:133], v[132:133], v[128:129] op_sel_hi:[1,0]
	s_nop 0
	v_mul_f32_e32 v129, 0xbfb8aa3b, v133
	v_exp_f32_e32 v129, v129
	s_nop 0
	v_add_f32_e32 v129, 1.0, v129
	v_rcp_f32_e32 v129, v129
	s_nop 0
	s_nop 0
	v_mul_f32_e32 v129, v133, v129
	v_mul_f32_e32 v141, v132, v129
	v_mov_b32_e32 v132, v126
	v_mov_b32_e32 v133, v10
	v_pk_mul_f32 v[132:133], v[132:133], v[128:129] op_sel_hi:[1,0]
	s_nop 0
	v_mul_f32_e32 v129, 0xbfb8aa3b, v133
	v_exp_f32_e32 v129, v129
	s_nop 0
	v_add_f32_e32 v129, 1.0, v129
	v_rcp_f32_e32 v129, v129
	s_nop 0
	s_nop 0
	v_mul_f32_e32 v129, v133, v129
	v_mul_f32_e32 v142, v132, v129
	v_mov_b32_e32 v132, v127
	v_mov_b32_e32 v133, v11
	v_pk_mul_f32 v[128:129], v[132:133], v[128:129] op_sel_hi:[1,0]
	s_nop 0
	v_mul_f32_e32 v132, 0xbfb8aa3b, v129
	v_exp_f32_e32 v132, v132
	s_nop 0
	v_add_f32_e32 v132, 1.0, v132
	v_rcp_f32_e32 v132, v132
	s_nop 0
	s_nop 0
	v_mul_f32_e32 v129, v129, v132
	v_mul_f32_e32 v143, v128, v129
	v_add_u32_e32 v128, s4, v188
	v_mad_i64_i32 v[128:129], s[2:3], v128, s5, v[130:131]
	v_lshl_add_u64 v[132:133], v[128:129], 0, v[134:135]
	v_cvt_pk_bf16_f32 v128, v136, v137
	v_cvt_pk_bf16_f32 v129, v138, v139
	v_cvt_pk_bf16_f32 v130, v140, v141
	v_cvt_pk_bf16_f32 v131, v142, v143
	s_nop 0
	global_store_dwordx4 v[132:133], v[128:131], off sc1
	s_nop 1
	s_waitcnt vmcnt(0)
	s_and_saveexec_b64 s[4:5], s[0:1]
	s_cbranch_execz .LBB0_1518
	s_mov_b64 s[26:27], exec
	v_mbcnt_lo_u32_b32 v128, s26, 0
	v_mbcnt_hi_u32_b32 v128, s27, v128
	v_cmp_eq_u32_e32 vcc, 0, v128
	s_and_b64 s[2:3], exec, vcc
	s_mov_b64 exec, s[2:3]
	s_cbranch_execz .LBB0_1518
	s_lshl_b32 s2, s44, 6
	s_ashr_i32 s3, s2, 31
	s_lshl_b64 s[2:3], s[2:3], 2
	s_add_u32 s2, s30, s2
	s_addc_u32 s3, s31, s3
	s_bcnt1_i32_b64 s8, s[26:27]
	v_mov_b32_e32 v128, s8
	global_atomic_add v161, v128, s[2:3]
